# deeper LDS prefetch of K fragments ahead of the QK MFMAs in the MoBA block attention (9-11 reads in flight instead of 2-4), same instruction results
# speedup vs baseline: 1.0034x; 1.0034x over previous
.LBB0_675:
	ds_read_b128 v[4:7], v221
	ds_read_b128 v[8:11], v221 offset:8192
	ds_read_b128 v[38:41], v222
	ds_read_b128 v[42:45], v222 offset:8192
	ds_read_b128 v[234:237], v223
	ds_read_b128 v[238:241], v223 offset:8192
	ds_read_b128 v[242:245], v224
	ds_read_b128 v[180:183], v224 offset:8192
	ds_read_b128 v[184:187], v225
	ds_read_b128 v[188:191], v225 offset:8192
	ds_read_b128 v[192:195], v226
	v_sub_u32_e32 v2, v36, v210
	v_cvt_f32_i32_e32 v46, v2
	s_waitcnt vmcnt(7) lgkmcnt(10)
	v_mfma_f32_32x32x16_bf16 v[20:35], v[4:7], v[100:103], 0
	s_cmp_gt_i32 s12, 7
	s_cselect_b64 s[40:41], -1, 0
	s_cmp_lt_i32 s12, 8
	s_mov_b64 s[8:9], -1
	s_waitcnt lgkmcnt(9)
	v_mfma_f32_32x32x16_bf16 v[4:19], v[8:11], v[100:103], 0
	s_waitcnt vmcnt(6) lgkmcnt(8)
	v_mfma_f32_32x32x16_bf16 v[20:35], v[38:41], v[104:107], v[20:35]
	ds_read_b128 v[38:41], v226 offset:8192
	s_waitcnt lgkmcnt(8)
	v_mfma_f32_32x32x16_bf16 v[4:19], v[42:45], v[104:107], v[4:19]
	ds_read_b128 v[42:45], v227
	s_waitcnt vmcnt(5) lgkmcnt(8)
	v_mfma_f32_32x32x16_bf16 v[20:35], v[234:237], v[108:111], v[20:35]
	ds_read_b128 v[234:237], v227 offset:8192
	s_waitcnt lgkmcnt(8)
	v_mfma_f32_32x32x16_bf16 v[4:19], v[238:241], v[108:111], v[4:19]
	ds_read_b128 v[238:241], v228
	s_waitcnt vmcnt(4) lgkmcnt(8)
	v_mfma_f32_32x32x16_bf16 v[20:35], v[242:245], v[118:121], v[20:35]
	ds_read_b128 v[242:245], v228 offset:8192
	s_waitcnt lgkmcnt(8)
	v_mfma_f32_32x32x16_bf16 v[4:19], v[180:183], v[118:121], v[4:19]
	s_waitcnt vmcnt(3) lgkmcnt(7)
	v_mfma_f32_32x32x16_bf16 v[20:35], v[184:187], v[122:125], v[20:35]
	s_waitcnt lgkmcnt(6)
	v_mfma_f32_32x32x16_bf16 v[4:19], v[188:191], v[122:125], v[4:19]
	s_waitcnt vmcnt(2) lgkmcnt(5)
	v_mfma_f32_32x32x16_bf16 v[20:35], v[192:195], v[126:129], v[20:35]
	s_waitcnt lgkmcnt(4)
	v_mfma_f32_32x32x16_bf16 v[4:19], v[38:41], v[126:129], v[4:19]
	s_waitcnt vmcnt(1) lgkmcnt(3)
	v_mfma_f32_32x32x16_bf16 v[20:35], v[42:45], v[130:133], v[20:35]
	s_waitcnt lgkmcnt(2)
	v_mfma_f32_32x32x16_bf16 v[4:19], v[234:237], v[130:133], v[4:19]
	s_waitcnt vmcnt(0) lgkmcnt(1)
	v_mfma_f32_32x32x16_bf16 v[20:35], v[238:241], v[134:137], v[20:35]
	s_waitcnt lgkmcnt(0)
	v_mfma_f32_32x32x16_bf16 v[4:19], v[242:245], v[134:137], v[4:19]
	s_cbranch_scc1 .LBB0_677
	v_add_f32_e32 v47, -1.0, v46
	v_pk_add_f32 v[50:51], v[46:47], s[92:93] op_sel_hi:[0,1]
	v_pk_add_f32 v[52:53], v[46:47], s[94:95] op_sel_hi:[0,1]
	v_pk_add_f32 v[56:57], v[46:47], s[48:49] op_sel_hi:[0,1]
	v_pk_add_f32 v[58:59], v[46:47], s[50:51] op_sel_hi:[0,1]
	v_pk_add_f32 v[62:63], v[46:47], s[52:53] op_sel_hi:[0,1]
	v_pk_add_f32 v[64:65], v[46:47], s[54:55] op_sel_hi:[0,1]
	v_pk_add_f32 v[70:71], v[46:47], s[56:57] op_sel_hi:[0,1]
	v_mov_b32_e32 v157, v156
	v_pk_add_f32 v[38:39], v[46:47], s[44:45] op_sel_hi:[1,0]
	v_pk_add_f32 v[40:41], v[50:51], s[44:45] op_sel_hi:[1,0]
	v_pk_add_f32 v[42:43], v[52:53], s[44:45] op_sel_hi:[1,0]
	v_pk_add_f32 v[44:45], v[56:57], s[44:45] op_sel_hi:[1,0]
	v_pk_add_f32 v[48:49], v[58:59], s[44:45] op_sel_hi:[1,0]
	v_pk_add_f32 v[54:55], v[62:63], s[44:45] op_sel_hi:[1,0]
	v_pk_add_f32 v[60:61], v[64:65], s[44:45] op_sel_hi:[1,0]
	v_add_f32_e32 v37, 0xc2000000, v70
	v_pk_fma_f32 v[66:67], v[156:157], v[64:65], v[32:33]
	v_pk_fma_f32 v[64:65], v[156:157], v[62:63], v[30:31]
	v_pk_fma_f32 v[62:63], v[156:157], v[58:59], v[28:29]
	v_pk_fma_f32 v[58:59], v[156:157], v[56:57], v[26:27]
	v_pk_fma_f32 v[56:57], v[156:157], v[52:53], v[24:25]
	v_pk_fma_f32 v[52:53], v[156:157], v[50:51], v[22:23]
	v_pk_fma_f32 v[50:51], v[162:163], v[46:47], v[20:21]
	v_add_f32_e32 v47, 0xc2000000, v71
	v_pk_fma_f32 v[38:39], v[160:161], v[38:39], v[4:5]
	v_pk_fma_f32 v[40:41], v[160:161], v[40:41], v[6:7]
	v_pk_fma_f32 v[42:43], v[160:161], v[42:43], v[8:9]
	v_pk_fma_f32 v[44:45], v[160:161], v[44:45], v[10:11]
	v_pk_fma_f32 v[48:49], v[160:161], v[48:49], v[12:13]
	v_pk_fma_f32 v[54:55], v[160:161], v[54:55], v[14:15]
	v_pk_fma_f32 v[60:61], v[160:161], v[60:61], v[16:17]
	v_fma_f32 v37, v156, v37, v18
	v_pk_fma_f32 v[68:69], v[156:157], v[70:71], v[34:35]
	v_fma_f32 v47, v156, v47, v19
	s_mov_b64 s[8:9], 0

.LBB0_682:
	v_add_u32_e32 v72, s13, v220
	v_add_u32_e32 v68, 0x14000, v72
	ds_read_b128 v[68:71], v68
	v_add_u32_e32 v72, 0x16000, v72
	ds_read_b128 v[72:75], v72
	v_add_u32_e32 v246, s13, v219
	v_add_u32_e32 v180, 0x14000, v246
	ds_read_b128 v[180:183], v180
	v_add_u32_e32 v184, 0x16000, v246
	ds_read_b128 v[184:187], v184
	v_add_u32_e32 v246, s13, v218
	v_add_u32_e32 v188, 0x14000, v246
	ds_read_b128 v[188:191], v188
	v_add_u32_e32 v192, 0x16000, v246
	ds_read_b128 v[192:195], v192
	v_add_u32_e32 v246, s13, v217
	v_add_u32_e32 v234, 0x14000, v246
	ds_read_b128 v[234:237], v234
	v_add_u32_e32 v238, 0x16000, v246
	ds_read_b128 v[238:241], v238
	v_add_u32_e32 v246, s13, v216
	v_add_u32_e32 v242, 0x14000, v246
	ds_read_b128 v[242:245], v242
	s_waitcnt lgkmcnt(8)
	v_mfma_f32_32x32x16_bf16 v[84:99], v[68:71], v[100:103], 0
	s_waitcnt lgkmcnt(7)
	v_mfma_f32_32x32x16_bf16 v[68:83], v[72:75], v[100:103], 0
	s_waitcnt lgkmcnt(6)
	v_mfma_f32_32x32x16_bf16 v[84:99], v[180:183], v[104:107], v[84:99]
	v_add_u32_e32 v180, 0x16000, v246
	ds_read_b128 v[180:183], v180
	s_waitcnt lgkmcnt(6)
	v_mfma_f32_32x32x16_bf16 v[68:83], v[184:187], v[104:107], v[68:83]
	v_add_u32_e32 v246, s13, v215
	v_add_u32_e32 v184, 0x14000, v246
	ds_read_b128 v[184:187], v184
	s_waitcnt lgkmcnt(6)
	v_mfma_f32_32x32x16_bf16 v[84:99], v[188:191], v[108:111], v[84:99]
	v_add_u32_e32 v188, 0x16000, v246
	ds_read_b128 v[188:191], v188
	s_waitcnt lgkmcnt(6)
	v_mfma_f32_32x32x16_bf16 v[68:83], v[192:195], v[108:111], v[68:83]
	v_add_u32_e32 v246, s13, v214
	v_add_u32_e32 v192, 0x14000, v246
	ds_read_b128 v[192:195], v192
	s_waitcnt lgkmcnt(6)
	v_mfma_f32_32x32x16_bf16 v[84:99], v[234:237], v[118:121], v[84:99]
	v_add_u32_e32 v234, 0x16000, v246
	ds_read_b128 v[234:237], v234
	s_waitcnt lgkmcnt(6)
	v_mfma_f32_32x32x16_bf16 v[68:83], v[238:241], v[118:121], v[68:83]
	v_add_u32_e32 v246, s13, v213
	v_add_u32_e32 v238, 0x14000, v246
	ds_read_b128 v[238:241], v238
	s_waitcnt lgkmcnt(6)
	v_mfma_f32_32x32x16_bf16 v[84:99], v[242:245], v[122:125], v[84:99]
	v_add_u32_e32 v242, 0x16000, v246
	ds_read_b128 v[242:245], v242
	s_waitcnt lgkmcnt(6)
	v_mfma_f32_32x32x16_bf16 v[68:83], v[180:183], v[122:125], v[68:83]
	s_waitcnt lgkmcnt(5)
	v_mfma_f32_32x32x16_bf16 v[84:99], v[184:187], v[126:129], v[84:99]
	s_waitcnt lgkmcnt(4)
	v_mfma_f32_32x32x16_bf16 v[68:83], v[188:191], v[126:129], v[68:83]
	s_waitcnt lgkmcnt(3)
	v_mfma_f32_32x32x16_bf16 v[84:99], v[192:195], v[130:133], v[84:99]
	s_waitcnt lgkmcnt(2)
	v_mfma_f32_32x32x16_bf16 v[68:83], v[234:237], v[130:133], v[68:83]
	v_add_u32_e32 v157, s13, v212
	s_waitcnt lgkmcnt(1)
	v_mfma_f32_32x32x16_bf16 v[84:99], v[238:241], v[134:137], v[84:99]
	ds_read_b64_tr_b16 v[180:181], v157 offset:0
	ds_read_b64_tr_b16 v[182:183], v157 offset:0x800
	s_waitcnt lgkmcnt(2)
	v_mfma_f32_32x32x16_bf16 v[68:83], v[242:245], v[134:137], v[68:83]
	ds_read_b64_tr_b16 v[184:185], v157 offset:0x1000
	ds_read_b64_tr_b16 v[186:187], v157 offset:0x1800
	ds_read_b64_tr_b16 v[188:189], v157 offset:0x2000
	ds_read_b64_tr_b16 v[190:191], v157 offset:0x2800
	ds_read_b64_tr_b16 v[192:193], v157 offset:0x3000
	ds_read_b64_tr_b16 v[194:195], v157 offset:0x3800
	s_waitcnt lgkmcnt(0)
	v_mfma_f32_32x32x16_bf16 v[20:35], v[180:183], v[138:141], v[20:35]
	ds_read_b64_tr_b16 v[180:181], v157 offset:0x200
	ds_read_b64_tr_b16 v[182:183], v157 offset:0xa00
	v_mfma_f32_32x32x16_bf16 v[20:35], v[184:187], v[142:145], v[20:35]
	ds_read_b64_tr_b16 v[184:185], v157 offset:0x1200
	ds_read_b64_tr_b16 v[186:187], v157 offset:0x1a00
	v_mfma_f32_32x32x16_bf16 v[20:35], v[188:191], v[146:149], v[20:35]
	ds_read_b64_tr_b16 v[188:189], v157 offset:0x2200
	ds_read_b64_tr_b16 v[190:191], v157 offset:0x2a00
	v_mfma_f32_32x32x16_bf16 v[20:35], v[192:195], v[150:153], v[20:35]
	ds_read_b64_tr_b16 v[192:193], v157 offset:0x3200
	ds_read_b64_tr_b16 v[194:195], v157 offset:0x3a00
	s_waitcnt lgkmcnt(0)
	v_mfma_f32_32x32x16_bf16 v[52:67], v[180:183], v[138:141], v[52:67]
	ds_read_b64_tr_b16 v[180:181], v157 offset:0x400
	ds_read_b64_tr_b16 v[182:183], v157 offset:0xc00
	v_mfma_f32_32x32x16_bf16 v[52:67], v[184:187], v[142:145], v[52:67]
	ds_read_b64_tr_b16 v[184:185], v157 offset:0x1400
	ds_read_b64_tr_b16 v[186:187], v157 offset:0x1c00
	v_mfma_f32_32x32x16_bf16 v[52:67], v[188:191], v[146:149], v[52:67]
	ds_read_b64_tr_b16 v[188:189], v157 offset:0x2400
	ds_read_b64_tr_b16 v[190:191], v157 offset:0x2c00
	v_mfma_f32_32x32x16_bf16 v[52:67], v[192:195], v[150:153], v[52:67]
	ds_read_b64_tr_b16 v[192:193], v157 offset:0x3400
	ds_read_b64_tr_b16 v[194:195], v157 offset:0x3c00
	s_waitcnt lgkmcnt(0)
	v_mfma_f32_32x32x16_bf16 v[36:51], v[180:183], v[138:141], v[36:51]
	ds_read_b64_tr_b16 v[180:181], v157 offset:0x600
	ds_read_b64_tr_b16 v[182:183], v157 offset:0xe00
	v_mfma_f32_32x32x16_bf16 v[36:51], v[184:187], v[142:145], v[36:51]
	ds_read_b64_tr_b16 v[184:185], v157 offset:0x1600
	ds_read_b64_tr_b16 v[186:187], v157 offset:0x1e00
	v_mfma_f32_32x32x16_bf16 v[36:51], v[188:191], v[146:149], v[36:51]
	ds_read_b64_tr_b16 v[188:189], v157 offset:0x2600
	ds_read_b64_tr_b16 v[190:191], v157 offset:0x2e00
	v_mfma_f32_32x32x16_bf16 v[36:51], v[192:195], v[150:153], v[36:51]
	ds_read_b64_tr_b16 v[192:193], v157 offset:0x3600
	ds_read_b64_tr_b16 v[194:195], v157 offset:0x3e00
	s_waitcnt lgkmcnt(0)
	v_mfma_f32_32x32x16_bf16 v[4:19], v[180:183], v[138:141], v[4:19]
	s_mov_b64 s[8:9], -1
	s_andn2_b64 vcc, exec, s[40:41]
	v_mfma_f32_32x32x16_bf16 v[4:19], v[184:187], v[142:145], v[4:19]
	v_mfma_f32_32x32x16_bf16 v[4:19], v[188:191], v[146:149], v[4:19]
	v_cvt_f32_i32_e32 v146, v113
	v_mfma_f32_32x32x16_bf16 v[4:19], v[192:195], v[150:153], v[4:19]
	s_cbranch_vccnz .LBB0_684
	v_add_f32_e32 v147, -1.0, v146
	v_pk_add_f32 v[232:233], v[146:147], s[56:57] op_sel_hi:[0,1]
	v_pk_add_f32 v[188:189], v[146:147], s[54:55] op_sel_hi:[0,1]
	v_add_f32_e32 v157, 0xc2000000, v232
	v_pk_add_f32 v[144:145], v[146:147], s[92:93] op_sel_hi:[0,1]
	v_pk_add_f32 v[150:151], v[146:147], s[94:95] op_sel_hi:[0,1]
	v_pk_add_f32 v[152:153], v[146:147], s[48:49] op_sel_hi:[0,1]
	v_pk_add_f32 v[182:183], v[146:147], s[50:51] op_sel_hi:[0,1]
	v_pk_add_f32 v[184:185], v[146:147], s[52:53] op_sel_hi:[0,1]
	v_pk_add_f32 v[190:191], v[188:189], s[44:45] op_sel_hi:[1,0]
	v_fma_f32 v230, v156, v157, v82
	v_mov_b32_e32 v157, v156
	v_pk_add_f32 v[138:139], v[146:147], s[44:45] op_sel_hi:[1,0]
	v_pk_add_f32 v[140:141], v[144:145], s[44:45] op_sel_hi:[1,0]
	v_pk_add_f32 v[142:143], v[150:151], s[44:45] op_sel_hi:[1,0]
	v_pk_add_f32 v[148:149], v[152:153], s[44:45] op_sel_hi:[1,0]
	v_pk_add_f32 v[180:181], v[182:183], s[44:45] op_sel_hi:[1,0]
	v_pk_add_f32 v[186:187], v[184:185], s[44:45] op_sel_hi:[1,0]
	v_pk_fma_f32 v[194:195], v[160:161], v[190:191], v[80:81]
	v_pk_fma_f32 v[190:191], v[156:157], v[188:189], v[96:97]
	v_pk_fma_f32 v[188:189], v[156:157], v[184:185], v[94:95]
	v_pk_fma_f32 v[184:185], v[156:157], v[182:183], v[92:93]
	v_pk_fma_f32 v[182:183], v[156:157], v[152:153], v[90:91]
	v_pk_fma_f32 v[152:153], v[156:157], v[150:151], v[88:89]
	v_pk_fma_f32 v[150:151], v[156:157], v[144:145], v[86:87]
	v_pk_fma_f32 v[144:145], v[162:163], v[146:147], v[84:85]
	v_add_f32_e32 v147, 0xc2000000, v233
	v_pk_fma_f32 v[138:139], v[160:161], v[138:139], v[68:69]
	v_pk_fma_f32 v[140:141], v[160:161], v[140:141], v[70:71]
	v_pk_fma_f32 v[142:143], v[160:161], v[142:143], v[72:73]
	v_pk_fma_f32 v[148:149], v[160:161], v[148:149], v[74:75]
	v_pk_fma_f32 v[180:181], v[160:161], v[180:181], v[76:77]
	v_pk_fma_f32 v[186:187], v[160:161], v[186:187], v[78:79]
	v_pk_fma_f32 v[192:193], v[156:157], v[232:233], v[98:99]
	v_fma_f32 v147, v156, v147, v83
	s_mov_b64 s[8:9], 0
